# P4 out-proj GEMM: dropped the compiler's conservative vmcnt(0) drain in front of the mid-K row-table LDS read (table is outside the DMA ring)
# speedup vs baseline: 1.0002x; 1.0002x over previous
; #define LAS __attribute__((address_space(3)))
; #define EPI_ROWS(...) _Pragma("unroll") for (int ai = 0; ai < 2; ++ai) _Pragma("unroll") for (int m = 0; m < 4; ++m) { const int rl = ai * 128 + wr * 64 + m * 16 + fr; const int row = u.pm * 256 + rl; (void)row; __VA_ARGS__ if (m & 1) asm volatile("" ::: "memory"); }
; template <int K, class Epi, class Sched, bool ALIGN_EPI>
; __device__ __forceinline__ void gemm_phase(LAS unsigned char* lds, const Gemm g, const Sched& S, const Epi& E) {
;     ...
;             if constexpr (Epi::HAS_MID) { if (t == nt / 2) E.mid(acc, cur, wr, wc, fr, fq, tab0 + (ui & 1) * 256); }
;     __device__ __forceinline__ void mid(AccT& acc, const Unit& u, int wr, int wc, int fr, int fq, const LAS f32x2* tab) const {
;         EPI_ROWS({ const float ratio = tab[rl].x;
; _Pragma("unroll")
;             for (int bj = 0; bj < 2; ++bj)
; _Pragma("unroll")
;                 for (int n = 0; n < 2; ++n) acc[ai][bj][m][n] *= ratio; })
.LBB0_1621:
	s_cmp_lg_u32 s1, s86
	s_cbranch_scc1 .LBB0_1620
	ds_read2_b32 v[132:133], v143 offset1:32
	v_add_u32_e32 v145, 0x400, v143
	s_waitcnt lgkmcnt(0)
	v_pk_mul_f32 v[118:119], v[118:119], v[132:133] op_sel_hi:[1,0]
	v_pk_mul_f32 v[116:117], v[116:117], v[132:133] op_sel_hi:[1,0]
	v_pk_mul_f32 v[122:123], v[122:123], v[132:133] op_sel_hi:[1,0]
	v_pk_mul_f32 v[120:121], v[120:121], v[132:133] op_sel_hi:[1,0]
	v_pk_mul_f32 v[140:141], v[140:141], v[132:133] op_sel_hi:[1,0]
	v_pk_mul_f32 v[138:139], v[138:139], v[132:133] op_sel_hi:[1,0]
	v_pk_mul_f32 v[126:127], v[126:127], v[132:133] op_sel_hi:[1,0]
	v_pk_mul_f32 v[124:125], v[124:125], v[132:133] op_sel_hi:[1,0]
	v_mov_b32_e32 v130, v133
	ds_read2_b32 v[132:133], v143 offset0:64 offset1:96
	v_pk_mul_f32 v[114:115], v[114:115], v[130:131] op_sel_hi:[1,0]
	v_pk_mul_f32 v[112:113], v[112:113], v[130:131] op_sel_hi:[1,0]
	v_pk_mul_f32 v[110:111], v[110:111], v[130:131] op_sel_hi:[1,0]
	v_pk_mul_f32 v[108:109], v[108:109], v[130:131] op_sel_hi:[1,0]
	v_pk_mul_f32 v[106:107], v[106:107], v[130:131] op_sel_hi:[1,0]
	v_pk_mul_f32 v[104:105], v[104:105], v[130:131] op_sel_hi:[1,0]
	v_pk_mul_f32 v[102:103], v[102:103], v[130:131] op_sel_hi:[1,0]
	v_pk_mul_f32 v[100:101], v[100:101], v[130:131] op_sel_hi:[1,0]
	s_waitcnt lgkmcnt(0)
	v_pk_mul_f32 v[98:99], v[98:99], v[132:133] op_sel_hi:[1,0]
	v_pk_mul_f32 v[96:97], v[96:97], v[132:133] op_sel_hi:[1,0]
	v_pk_mul_f32 v[94:95], v[94:95], v[132:133] op_sel_hi:[1,0]
	v_pk_mul_f32 v[92:93], v[92:93], v[132:133] op_sel_hi:[1,0]
	v_pk_mul_f32 v[90:91], v[90:91], v[132:133] op_sel_hi:[1,0]
	v_pk_mul_f32 v[88:89], v[88:89], v[132:133] op_sel_hi:[1,0]
	v_pk_mul_f32 v[86:87], v[86:87], v[132:133] op_sel_hi:[1,0]
	v_pk_mul_f32 v[84:85], v[84:85], v[132:133] op_sel_hi:[1,0]
	v_mov_b32_e32 v130, v133
	ds_read2_b32 v[132:133], v145 offset1:32
	v_pk_mul_f32 v[82:83], v[82:83], v[130:131] op_sel_hi:[1,0]
	v_pk_mul_f32 v[80:81], v[80:81], v[130:131] op_sel_hi:[1,0]
	v_pk_mul_f32 v[78:79], v[78:79], v[130:131] op_sel_hi:[1,0]
	v_pk_mul_f32 v[76:77], v[76:77], v[130:131] op_sel_hi:[1,0]
	v_pk_mul_f32 v[74:75], v[74:75], v[130:131] op_sel_hi:[1,0]
	v_pk_mul_f32 v[72:73], v[72:73], v[130:131] op_sel_hi:[1,0]
	v_pk_mul_f32 v[70:71], v[70:71], v[130:131] op_sel_hi:[1,0]
	v_pk_mul_f32 v[68:69], v[68:69], v[130:131] op_sel_hi:[1,0]
	s_waitcnt lgkmcnt(0)
	v_pk_mul_f32 v[62:63], v[62:63], v[132:133] op_sel_hi:[1,0]
	v_pk_mul_f32 v[60:61], v[60:61], v[132:133] op_sel_hi:[1,0]
	v_pk_mul_f32 v[66:67], v[66:67], v[132:133] op_sel_hi:[1,0]
	v_pk_mul_f32 v[64:65], v[64:65], v[132:133] op_sel_hi:[1,0]
	v_pk_mul_f32 v[58:59], v[58:59], v[132:133] op_sel_hi:[1,0]
	v_pk_mul_f32 v[56:57], v[56:57], v[132:133] op_sel_hi:[1,0]
	v_pk_mul_f32 v[54:55], v[54:55], v[132:133] op_sel_hi:[1,0]
	v_pk_mul_f32 v[52:53], v[52:53], v[132:133] op_sel_hi:[1,0]
	v_mov_b32_e32 v130, v133
	ds_read2_b32 v[132:133], v145 offset0:64 offset1:96
	v_pk_mul_f32 v[50:51], v[50:51], v[130:131] op_sel_hi:[1,0]
	v_pk_mul_f32 v[48:49], v[48:49], v[130:131] op_sel_hi:[1,0]
	v_pk_mul_f32 v[46:47], v[46:47], v[130:131] op_sel_hi:[1,0]
	v_pk_mul_f32 v[44:45], v[44:45], v[130:131] op_sel_hi:[1,0]
	v_pk_mul_f32 v[42:43], v[42:43], v[130:131] op_sel_hi:[1,0]
	v_pk_mul_f32 v[40:41], v[40:41], v[130:131] op_sel_hi:[1,0]
	v_pk_mul_f32 v[38:39], v[38:39], v[130:131] op_sel_hi:[1,0]
	v_pk_mul_f32 v[36:37], v[36:37], v[130:131] op_sel_hi:[1,0]
	s_waitcnt lgkmcnt(0)
	v_mov_b32_e32 v130, v133
	v_pk_mul_f32 v[34:35], v[34:35], v[132:133] op_sel_hi:[1,0]
	v_pk_mul_f32 v[32:33], v[32:33], v[132:133] op_sel_hi:[1,0]
	v_pk_mul_f32 v[30:31], v[30:31], v[132:133] op_sel_hi:[1,0]
	v_pk_mul_f32 v[28:29], v[28:29], v[132:133] op_sel_hi:[1,0]
	v_pk_mul_f32 v[26:27], v[26:27], v[132:133] op_sel_hi:[1,0]
	v_pk_mul_f32 v[24:25], v[24:25], v[132:133] op_sel_hi:[1,0]
	v_pk_mul_f32 v[22:23], v[22:23], v[132:133] op_sel_hi:[1,0]
	v_pk_mul_f32 v[20:21], v[20:21], v[132:133] op_sel_hi:[1,0]
	v_pk_mul_f32 v[18:19], v[18:19], v[130:131] op_sel_hi:[1,0]
	v_pk_mul_f32 v[16:17], v[16:17], v[130:131] op_sel_hi:[1,0]
	v_pk_mul_f32 v[14:15], v[14:15], v[130:131] op_sel_hi:[1,0]
	v_pk_mul_f32 v[12:13], v[12:13], v[130:131] op_sel_hi:[1,0]
	v_pk_mul_f32 v[10:11], v[10:11], v[130:131] op_sel_hi:[1,0]
	v_pk_mul_f32 v[8:9], v[8:9], v[130:131] op_sel_hi:[1,0]
	v_pk_mul_f32 v[6:7], v[6:7], v[130:131] op_sel_hi:[1,0]
	v_pk_mul_f32 v[4:5], v[4:5], v[130:131] op_sel_hi:[1,0]
	s_branch .LBB0_1620
